# v048 + P0 xq four-row wave-max reductions rewritten with DPP (no ds_bpermute)
# baseline (speedup 1.0000x reference)
; __device__ __forceinline__ int xq_ticket(unsigned* ctr, int lane) { int q = 0; if (lane == 0) q = (int)__hip_atomic_fetch_add(ctr, 1u, __ATOMIC_RELAXED, __HIP_MEMORY_SCOPE_AGENT); return __builtin_amdgcn_readfirstlane(q); }
; __device__ __forceinline__ void xq_rows(const float* x, bf16_t* xb, unsigned char* x8, float* sxx, unsigned* ctr, int qbase, int qcount, int lane) {
;     ...
;         const int r0 = (qbase + qn) * XR;
;         qn = xq_ticket(ctr, lane);
;         f32x4 a[XR][4], c[XR][4];
; #pragma unroll
;         for (int rr = 0; rr < XR; ++rr)
; #pragma unroll
;             for (int j = 0; j < 4; ++j) { const f32x4* p = (const f32x4*)(x + (size_t)(r0 + rr) * D_ + j * 512 + lane * 8); a[rr][j] = __builtin_nontemporal_load(p); c[rr][j] = __builtin_nontemporal_load(p + 1); }
;         float amax[XR];
; #pragma unroll
;         for (int rr = 0; rr < XR; ++rr) { amax[rr] = 0.f;
; #pragma unroll
;             for (int j = 0; j < 4; ++j) { amax[rr] = fmaxf(amax[rr], fmaxf(fmaxf(fabsf(a[rr][j].x), fabsf(a[rr][j].y)), fmaxf(fabsf(a[rr][j].z), fabsf(a[rr][j].w))));
;                                           amax[rr] = fmaxf(amax[rr], fmaxf(fmaxf(fabsf(c[rr][j].x), fabsf(c[rr][j].y)), fmaxf(fabsf(c[rr][j].z), fabsf(c[rr][j].w)))); } }
.LBB0_59:
	s_or_b64 exec, exec, s[10:11]
	s_add_i32 s10, s16, s3
	s_lshl_b32 s16, s10, 2
	s_ashr_i32 s17, s16, 31
	s_lshl_b64 s[10:11], s[16:17], 13
	v_lshl_add_u64 v[2:3], v[134:135], 0, s[10:11]
	v_add_co_u32_e32 v4, vcc, s20, v2
	global_load_dwordx4 v[126:129], v[2:3], off nt
	global_load_dwordx4 v[122:125], v[2:3], off offset:16 nt
	global_load_dwordx4 v[118:121], v[2:3], off offset:2048 nt
	global_load_dwordx4 v[114:117], v[2:3], off offset:2064 nt
	v_addc_co_u32_e32 v5, vcc, 0, v3, vcc
	global_load_dwordx4 v[110:113], v[4:5], off nt
	v_lshl_add_u64 v[6:7], v[2:3], 0, s[6:7]
	global_load_dwordx4 v[106:109], v[6:7], off offset:16 nt
	global_load_dwordx4 v[102:105], v[4:5], off offset:2048 nt
	v_lshl_add_u64 v[2:3], v[2:3], 0, s[8:9]
	global_load_dwordx4 v[98:101], v[2:3], off offset:16 nt
	s_or_b32 s14, s16, 1
	s_ashr_i32 s15, s14, 31
	s_lshl_b64 s[10:11], s[14:15], 13
	v_lshl_add_u64 v[2:3], v[134:135], 0, s[10:11]
	global_load_dwordx4 v[78:81], v[2:3], off nt
	global_load_dwordx4 v[66:69], v[2:3], off offset:16 nt
	global_load_dwordx4 v[58:61], v[2:3], off offset:2064 nt
	global_load_dwordx4 v[74:77], v[2:3], off offset:2048 nt
	s_or_b32 s12, s16, 2
	s_ashr_i32 s13, s12, 31
	s_lshl_b64 s[18:19], s[12:13], 13
	v_lshl_add_u64 v[4:5], v[134:135], 0, s[18:19]
	v_add_co_u32_e32 v14, vcc, s20, v2
	v_lshl_add_u64 v[6:7], v[2:3], 0, s[6:7]
	s_nop 0
	v_addc_co_u32_e32 v15, vcc, 0, v3, vcc
	global_load_dwordx4 v[38:41], v[4:5], off offset:16 nt
	global_load_dwordx4 v[42:45], v[4:5], off nt
	global_load_dwordx4 v[94:97], v[14:15], off nt
	global_load_dwordx4 v[26:29], v[4:5], off offset:2064 nt
	global_load_dwordx4 v[34:37], v[4:5], off offset:2048 nt
	global_load_dwordx4 v[90:93], v[6:7], off offset:16 nt
	s_or_b32 s10, s16, 3
	s_ashr_i32 s11, s10, 31
	s_lshl_b64 s[24:25], s[10:11], 13
	v_add_co_u32_e32 v20, vcc, s20, v4
	v_lshl_add_u64 v[62:63], v[134:135], 0, s[24:25]
	v_lshl_add_u64 v[16:17], v[2:3], 0, s[8:9]
	v_lshl_add_u64 v[18:19], v[4:5], 0, s[6:7]
	v_addc_co_u32_e32 v21, vcc, 0, v5, vcc
	v_lshl_add_u64 v[46:47], v[4:5], 0, s[8:9]
	global_load_dwordx4 v[6:9], v[62:63], off offset:16 nt
	global_load_dwordx4 v[10:13], v[62:63], off nt
	global_load_dwordx4 v[2:5], v[62:63], off offset:2048 nt
	global_load_dwordx4 v[86:89], v[14:15], off offset:2048 nt
	global_load_dwordx4 v[82:85], v[16:17], off offset:16 nt
	global_load_dwordx4 v[30:33], v[20:21], off nt
	global_load_dwordx4 v[22:25], v[18:19], off offset:16 nt
	s_nop 0
	global_load_dwordx4 v[18:21], v[20:21], off offset:2048 nt
	s_nop 0
	global_load_dwordx4 v[14:17], v[46:47], off offset:16 nt
	v_add_co_u32_e32 v64, vcc, s20, v62
	s_waitcnt vmcnt(26)
	v_max_f32_e64 v46, |v129|, |v129|
	v_max_f32_e64 v47, |v128|, |v128|
	s_waitcnt vmcnt(25)
	v_max_f32_e64 v48, |v125|, |v125|
	v_max_f32_e64 v49, |v124|, |v124|
	s_waitcnt vmcnt(24)
	v_max_f32_e64 v50, |v121|, |v121|
	v_max_f32_e64 v51, |v120|, |v120|
	s_waitcnt vmcnt(23)
	v_max_f32_e64 v52, |v117|, |v117|
	v_max_f32_e64 v53, |v116|, |v116|
	v_max_f32_e32 v46, v47, v46
	v_max_f32_e32 v47, v49, v48
	v_max_f32_e32 v48, v51, v50
	v_max_f32_e32 v49, v53, v52
	v_max3_f32 v46, |v126|, |v127|, v46
	v_max3_f32 v47, |v122|, |v123|, v47
	s_waitcnt vmcnt(22)
	v_max_f32_e64 v50, |v113|, |v113|
	v_max_f32_e64 v51, |v112|, |v112|
	s_waitcnt vmcnt(21)
	v_max_f32_e64 v52, |v109|, |v109|
	v_max_f32_e64 v53, |v108|, |v108|
	v_max3_f32 v48, |v118|, |v119|, v48
	v_max3_f32 v49, |v114|, |v115|, v49
	v_max3_f32 v46, v46, 0, v47
	v_max_f32_e32 v47, v51, v50
	v_max_f32_e32 v50, v53, v52
	v_max3_f32 v46, v46, v48, v49
	v_max3_f32 v47, |v110|, |v111|, v47
	v_max3_f32 v48, |v106|, |v107|, v50
	s_waitcnt vmcnt(20)
	v_max_f32_e64 v54, |v105|, |v105|
	v_max3_f32 v46, v46, v47, v48
	v_max_f32_e64 v47, |v104|, |v104|
	s_waitcnt vmcnt(19)
	v_max_f32_e64 v48, |v101|, |v101|
	v_max_f32_e64 v49, |v100|, |v100|
	v_max_f32_e32 v47, v47, v54
	v_max_f32_e32 v48, v49, v48
	v_max3_f32 v47, |v102|, |v103|, v47
	v_max3_f32 v48, |v98|, |v99|, v48
	v_max3_f32 v143, v46, v47, v48
	s_waitcnt vmcnt(18)
	v_max_f32_e64 v46, |v81|, |v81|
	v_max_f32_e64 v47, |v80|, |v80|
	v_max_f32_e32 v46, v47, v46
	s_waitcnt vmcnt(17)
	v_max_f32_e64 v47, |v69|, |v69|
	v_max_f32_e64 v48, |v68|, |v68|
	v_max_f32_e32 v47, v48, v47
	v_max3_f32 v46, |v78|, |v79|, v46
	v_max3_f32 v47, |v66|, |v67|, v47
	v_max3_f32 v70, v46, 0, v47
	s_waitcnt vmcnt(15)
	v_max_f32_e64 v46, |v77|, |v77|
	v_max_f32_e64 v47, |v76|, |v76|
	global_load_dwordx4 v[50:53], v[62:63], off offset:2064 nt
	v_max_f32_e32 v46, v47, v46
	v_max3_f32 v71, |v74|, |v75|, v46
	v_lshl_add_u64 v[46:47], v[62:63], 0, s[6:7]
	v_addc_co_u32_e32 v65, vcc, 0, v63, vcc
	global_load_dwordx4 v[46:49], v[46:47], off offset:16 nt
	s_nop 0
	global_load_dwordx4 v[54:57], v[64:65], off nt
	v_max_f32_e64 v72, |v61|, |v61|
	v_max_f32_e64 v73, |v60|, |v60|
	v_max_f32_e32 v72, v73, v72
	v_max3_f32 v72, |v58|, |v59|, v72
	v_max3_f32 v144, v70, v71, v72
	s_waitcnt vmcnt(15)
	v_max_f32_e64 v70, |v97|, |v97|
	v_max_f32_e64 v71, |v96|, |v96|
	v_max_f32_e32 v70, v71, v70
	v_max3_f32 v145, |v94|, |v95|, v70
	s_waitcnt vmcnt(12)
	v_max_f32_e64 v70, |v93|, |v93|
	v_max_f32_e64 v71, |v92|, |v92|
	v_max_f32_e32 v70, v71, v70
	v_max3_f32 v146, |v90|, |v91|, v70
	global_load_dwordx4 v[70:73], v[64:65], off offset:2048 nt
	v_lshl_add_u64 v[62:63], v[62:63], 0, s[8:9]
	global_load_dwordx4 v[62:65], v[62:63], off offset:16 nt
	v_max3_f32 v144, v144, v145, v146
	s_waitcnt vmcnt(10)
; __device__ __forceinline__ void xq_rows(const float* x, bf16_t* xb, unsigned char* x8, float* sxx, unsigned* ctr, int qbase, int qcount, int lane) {
;     ...
;         float amax[XR];
; #pragma unroll
;         for (int rr = 0; rr < XR; ++rr) { amax[rr] = 0.f;
; #pragma unroll
;             for (int j = 0; j < 4; ++j) { amax[rr] = fmaxf(amax[rr], fmaxf(fmaxf(fabsf(a[rr][j].x), fabsf(a[rr][j].y)), fmaxf(fabsf(a[rr][j].z), fabsf(a[rr][j].w))));
;                                           amax[rr] = fmaxf(amax[rr], fmaxf(fmaxf(fabsf(c[rr][j].x), fabsf(c[rr][j].y)), fmaxf(fabsf(c[rr][j].z), fabsf(c[rr][j].w)))); } }
; #pragma unroll
;         for (int rr = 0; rr < XR; ++rr) amax[rr] = wave_max(amax[rr]);
; #pragma unroll
;         for (int rr = 0; rr < XR; ++rr) {
;             const float inv = amax[rr] > 0.f ? 127.0f / amax[rr] : 0.f;
;             const int r = r0 + rr;
;             if (lane == 0) sxx[r] = amax[rr] * (1.0f / 127.0f);
	v_max_f32_e64 v145, |v89|, |v89|
	v_max_f32_e64 v146, |v88|, |v88|
	v_max_f32_e32 v145, v146, v145
	s_waitcnt vmcnt(9)
	v_max_f32_e64 v146, |v85|, |v85|
	v_max_f32_e64 v147, |v84|, |v84|
	v_max_f32_e32 v146, v147, v146
	v_max3_f32 v145, |v86|, |v87|, v145
	v_max3_f32 v146, |v82|, |v83|, v146
	v_max3_f32 v144, v144, v145, v146
	v_max_f32_e64 v145, |v45|, |v45|
	v_max_f32_e64 v146, |v44|, |v44|
	v_max_f32_e32 v145, v146, v145
	v_max_f32_e64 v146, |v41|, |v41|
	v_max_f32_e64 v147, |v40|, |v40|
	v_max_f32_e32 v146, v147, v146
	v_max3_f32 v145, |v42|, |v43|, v145
	v_max3_f32 v146, |v38|, |v39|, v146
	v_max3_f32 v145, v145, 0, v146
	v_max_f32_e64 v146, |v37|, |v37|
	v_max_f32_e64 v147, |v36|, |v36|
	v_max_f32_e32 v146, v147, v146
	v_max_f32_e64 v147, |v29|, |v29|
	v_max_f32_e64 v148, |v28|, |v28|
	v_max_f32_e32 v147, v148, v147
	v_max3_f32 v146, |v34|, |v35|, v146
	v_max3_f32 v147, |v26|, |v27|, v147
	v_max3_f32 v145, v145, v146, v147
	s_waitcnt vmcnt(8)
	v_max_f32_e64 v146, |v33|, |v33|
	v_max_f32_e64 v147, |v32|, |v32|
	v_max_f32_e32 v146, v147, v146
	s_waitcnt vmcnt(7)
	v_max_f32_e64 v147, |v25|, |v25|
	v_max_f32_e64 v148, |v24|, |v24|
	v_max_f32_e32 v147, v148, v147
	v_max3_f32 v146, |v30|, |v31|, v146
	v_max3_f32 v147, |v22|, |v23|, v147
	v_max3_f32 v145, v145, v146, v147
	s_waitcnt vmcnt(6)
	v_max_f32_e64 v146, |v21|, |v21|
	v_max_f32_e64 v147, |v20|, |v20|
	v_max_f32_e32 v146, v147, v146
	s_waitcnt vmcnt(5)
	v_max_f32_e64 v147, |v17|, |v17|
	v_max_f32_e64 v148, |v16|, |v16|
	v_max_f32_e32 v147, v148, v147
	v_max3_f32 v146, |v18|, |v19|, v146
	v_max3_f32 v147, |v14|, |v15|, v147
	v_max3_f32 v145, v145, v146, v147
	v_max_f32_e64 v146, |v13|, |v13|
	v_max_f32_e64 v147, |v12|, |v12|
	v_max_f32_e32 v146, v147, v146
	v_max_f32_e64 v147, |v9|, |v9|
	v_max_f32_e64 v148, |v8|, |v8|
	v_max_f32_e32 v147, v148, v147
	v_max3_f32 v146, |v10|, |v11|, v146
	v_max3_f32 v147, |v6|, |v7|, v147
	v_max3_f32 v146, v146, 0, v147
	v_max_f32_e64 v147, |v5|, |v5|
	v_max_f32_e64 v148, |v4|, |v4|
	v_max_f32_e32 v147, v148, v147
	s_waitcnt vmcnt(4)
	v_max_f32_e64 v148, |v53|, |v53|
	v_max_f32_e64 v149, |v52|, |v52|
	v_max_f32_e32 v148, v149, v148
	v_max3_f32 v147, |v2|, |v3|, v147
	v_max3_f32 v148, |v50|, |v51|, v148
	s_nop 1
	v_max_f32_dpp v143, v143, v143 quad_perm:[1,0,3,2] row_mask:0xf bank_mask:0xf
	v_max_f32_dpp v144, v144, v144 quad_perm:[1,0,3,2] row_mask:0xf bank_mask:0xf
	v_max_f32_dpp v145, v145, v145 quad_perm:[1,0,3,2] row_mask:0xf bank_mask:0xf
	v_max_f32_dpp v143, v143, v143 quad_perm:[2,3,0,1] row_mask:0xf bank_mask:0xf
	v_max_f32_dpp v144, v144, v144 quad_perm:[2,3,0,1] row_mask:0xf bank_mask:0xf
	v_max_f32_dpp v145, v145, v145 quad_perm:[2,3,0,1] row_mask:0xf bank_mask:0xf
	v_max_f32_dpp v143, v143, v143 row_half_mirror row_mask:0xf bank_mask:0xf
	v_max_f32_dpp v144, v144, v144 row_half_mirror row_mask:0xf bank_mask:0xf
	v_max_f32_dpp v145, v145, v145 row_half_mirror row_mask:0xf bank_mask:0xf
	v_max_f32_dpp v143, v143, v143 row_mirror row_mask:0xf bank_mask:0xf
	v_max_f32_dpp v144, v144, v144 row_mirror row_mask:0xf bank_mask:0xf
	v_max_f32_dpp v145, v145, v145 row_mirror row_mask:0xf bank_mask:0xf
	v_max_f32_dpp v143, v143, v143 row_bcast:15 row_mask:0xa bank_mask:0xf
	v_max_f32_dpp v144, v144, v144 row_bcast:15 row_mask:0xa bank_mask:0xf
	v_max_f32_dpp v145, v145, v145 row_bcast:15 row_mask:0xa bank_mask:0xf
	v_max_f32_dpp v143, v143, v143 row_bcast:31 row_mask:0xc bank_mask:0xf
	v_max_f32_dpp v144, v144, v144 row_bcast:31 row_mask:0xc bank_mask:0xf
	v_max_f32_dpp v145, v145, v145 row_bcast:31 row_mask:0xc bank_mask:0xf
	s_nop 1
	v_readlane_b32 s98, v143, 63
	v_readlane_b32 s99, v144, 63
	v_readlane_b32 s18, v145, 63
	v_max3_f32 v146, v146, v147, v148
	s_waitcnt vmcnt(2)
	v_max_f32_e64 v147, |v57|, |v57|
	v_max_f32_e64 v148, |v56|, |v56|
	v_max_f32_e32 v147, v148, v147
	v_max_f32_e64 v148, |v49|, |v49|
	v_max_f32_e64 v149, |v48|, |v48|
	v_max_f32_e32 v148, v149, v148
	v_max3_f32 v147, |v54|, |v55|, v147
	v_max3_f32 v148, |v46|, |v47|, v148
	v_max3_f32 v146, v146, v147, v148
	s_waitcnt vmcnt(1)
	v_max_f32_e64 v148, |v73|, |v73|
	v_max_f32_e64 v149, |v72|, |v72|
	v_max_f32_e32 v148, v149, v148
	s_waitcnt vmcnt(0)
	v_max_f32_e64 v149, |v65|, |v65|
	v_max_f32_e64 v150, |v64|, |v64|
	v_max_f32_e32 v149, v150, v149
	v_max3_f32 v148, |v70|, |v71|, v148
	v_max3_f32 v149, |v62|, |v63|, v149
	v_max3_f32 v146, v146, v148, v149
	s_nop 1
	v_max_f32_dpp v146, v146, v146 quad_perm:[1,0,3,2] row_mask:0xf bank_mask:0xf
	s_nop 1
	v_max_f32_dpp v146, v146, v146 quad_perm:[2,3,0,1] row_mask:0xf bank_mask:0xf
	s_nop 1
	v_max_f32_dpp v146, v146, v146 row_half_mirror row_mask:0xf bank_mask:0xf
	s_nop 1
	v_max_f32_dpp v146, v146, v146 row_mirror row_mask:0xf bank_mask:0xf
	s_nop 1
	v_max_f32_dpp v146, v146, v146 row_bcast:15 row_mask:0xa bank_mask:0xf
	s_nop 1
	v_max_f32_dpp v146, v146, v146 row_bcast:31 row_mask:0xc bank_mask:0xf
	s_nop 1
	v_readlane_b32 s19, v146, 63
	v_mov_b32_e32 v148, s98
	v_mov_b32_e32 v147, s99
	v_mov_b32_e32 v149, s99
	v_mov_b32_e32 v145, s18
	v_mov_b32_e32 v146, s18
	v_mov_b32_e32 v143, s19
	v_mov_b32_e32 v144, s19
	s_waitcnt lgkmcnt(0)
	s_and_saveexec_b64 s[18:19], s[4:5]
	s_cbranch_execz .LBB0_61
	s_lshl_b64 s[24:25], s[16:17], 2
	s_add_u32 s24, s46, s24
	s_addc_u32 s25, s47, s25
	v_mul_f32_e32 v150, 0x3c010204, v148
	global_store_dword v133, v150, s[24:25]
